# C1 step top: counted waits leave the previous step's state-tile stores and the next V^T request in flight (they were drained with the awaited log-decay loads)
# speedup vs baseline: 1.0086x; 1.0086x over previous
; #define LAS __attribute__((address_space(3)))
; __device__ __forceinline__ int tid_hidden() { int t = threadIdx.x; asm volatile("" : "+v"(t)); return t; }
; #define C1_PF_LF(ITEM, DIR) do { const int b_ = (ITEM) >> 7, h_ = ((ITEM) >> 5) & 3, j_ = (ITEM) & 31; const size_t tk_ = (size_t)b_ * SEQ + j_ * 64; \
;         _Pragma("unroll") for (int i = 0; i < 16; ++i) lfn[i] = (unsigned)((const unsigned short*)LF)[(tk_ + tq * 16 + i) * 1024 + (DIR) * 512 + h_ * 128 + d]; } while (0)
; #define C1_PF_VT(ITEM) do { const int b_ = (ITEM) >> 7, h_ = ((ITEM) >> 5) & 3, j_ = (ITEM) & 31; \
;         _Pragma("unroll") for (int i = 0; i < 2; ++i) { const int ch = tid + i * 512, e = ch >> 3, part = ch & 7; vtn[i] = *(const u32x4*)(VTH + ((size_t)b_ * 512 + h_ * 128 + e) * SEQ + j_ * 64 + part * 8); } } while (0)
; #define lds lds_hidden(lds0)
; #define DEC WSP(float, W_DEC)
; __device__ __forceinline__ void c1_phase(LAS unsigned char* lds, const bf16_t* __restrict__ LF, const bf16_t* __restrict__ VTH, bf16_t* __restrict__ UT, float* __restrict__ DEC, int first, int count, int stride) {
;     const int tid = tid_hidden(), wid = __builtin_amdgcn_readfirstlane(tid >> 6), lane = tid & 63, l15 = lane & 15, g4 = lane >> 4;
;     const int d = tid & 127, tq = tid >> 7;
;     LAS float* qtot = (LAS float*)(lds + C1_QT);
;     unsigned lfn[16]; u32x4 vtn[2];
;     ...
;     if (count > 0) { C1_PF_VT(first); C1_PF_LF(first, 0); }
.Lcn_done:
	s_andn2_b32 s36, s36, 63
	s_mov_b64 s[2:3], s[86:87]
	s_waitcnt lgkmcnt(0)
	s_add_u32 s0, s0, 0xc808000
	s_addc_u32 s1, s1, 0
	s_load_dwordx2 s[2:3], s[2:3], 0xa8
	s_mov_b64 s[6:7], s[86:87]
	s_waitcnt vmcnt(0)
	v_mov_b32_e32 v255, 0
	v_mov_b32_e32 v10, v0
	v_mov_b32_e32 v15, v35
	v_mov_b32_e32 v11, v35
	s_waitcnt lgkmcnt(0)
	s_add_u32 s4, s2, 0x10808000
	s_addc_u32 s5, s3, 0
	s_load_dwordx2 s[2:3], s[6:7], 0xa8
	s_mov_b64 s[6:7], s[86:87]
	s_mov_b32 s19, 0
	s_waitcnt lgkmcnt(0)
	s_add_u32 s2, s2, 0x13888000
	s_addc_u32 s3, s3, 0
	s_load_dwordx2 s[6:7], s[6:7], 0xa8
	s_waitcnt lgkmcnt(0)
	s_add_u32 s12, s6, 0x1b888000
	s_addc_u32 s13, s7, 0
	s_ashr_i32 s6, s28, 7
	s_lshl_b32 s10, s28, 2
	s_ashr_i32 s7, s6, 31
	s_and_b32 s15, s10, 0x180
	s_lshl_b32 s10, s28, 6
	s_lshl_b64 s[8:9], s[6:7], 9
	s_and_b32 s16, s10, 0x7c0
	s_or_b32 s8, s8, s15
	s_lshl_b32 s10, s16, 1
	s_add_u32 s10, s4, s10
	v_ashrrev_i32_e32 v36, 7, v10
	s_addc_u32 s11, s5, 0
	s_lshl_b64 s[6:7], s[6:7], 11
	v_lshlrev_b32_e32 v22, 4, v36
	s_or_b32 s6, s6, s16
	v_ashrrev_i32_e32 v23, 31, v22
	v_lshl_add_u64 v[12:13], s[6:7], 0, v[22:23]
	s_lshl_b32 s6, s15, 1
	v_and_b32_e32 v37, 0x7f, v10
	s_add_u32 s6, s0, s6
	s_addc_u32 s7, s1, 0
	v_lshlrev_b32_e32 v14, 1, v37
	v_lshl_add_u64 v[16:17], s[6:7], 0, v[14:15]
	v_lshlrev_b64 v[12:13], 11, v[12:13]
	v_lshl_add_u64 v[12:13], v[16:17], 0, v[12:13]
	s_movk_i32 s6, 0x1000
	v_add_co_u32_e32 v16, vcc, s6, v12
	s_movk_i32 s6, 0x3000
	s_nop 0
	v_addc_co_u32_e32 v17, vcc, 0, v13, vcc
	v_add_co_u32_e32 v24, vcc, s83, v12
	v_add_u32_e32 v6, 0x200, v10
	s_nop 0
	v_addc_co_u32_e32 v25, vcc, 0, v13, vcc
	v_add_co_u32_e32 v26, vcc, s6, v12
	v_ashrrev_i32_e32 v18, 3, v10
	s_nop 0
	v_addc_co_u32_e32 v27, vcc, 0, v13, vcc
	v_add_co_u32_e32 v28, vcc, s92, v12
	v_ashrrev_i32_e32 v20, 3, v6
	s_nop 0
	v_addc_co_u32_e32 v29, vcc, 0, v13, vcc
	s_movk_i32 s6, 0x5000
	v_lshlrev_b32_e32 v2, 4, v10
	v_ashrrev_i32_e32 v19, 31, v18
	v_ashrrev_i32_e32 v21, 31, v20
	v_add_co_u32_e32 v30, vcc, s6, v12
	v_and_b32_e32 v34, 0x70, v2
	v_lshl_add_u64 v[4:5], s[8:9], 0, v[18:19]
	v_lshl_add_u64 v[6:7], s[8:9], 0, v[20:21]
	v_addc_co_u32_e32 v31, vcc, 0, v13, vcc
	v_lshl_add_u64 v[2:3], s[10:11], 0, v[34:35]
	v_lshlrev_b64 v[4:5], 12, v[4:5]
	v_lshlrev_b64 v[6:7], 12, v[6:7]
	v_add_co_u32_e32 v32, vcc, s93, v12
	v_lshl_add_u64 v[4:5], v[2:3], 0, v[4:5]
	v_lshl_add_u64 v[6:7], v[2:3], 0, v[6:7]
	v_addc_co_u32_e32 v33, vcc, 0, v13, vcc
	s_movk_i32 s6, 0x7000
	global_load_dwordx4 v[2:5], v[4:5], off
	s_nop 0
	global_load_dwordx4 v[6:9], v[6:7], off
	s_nop 0
	global_load_ushort v109, v[24:25], off
	global_load_ushort v108, v[24:25], off offset:2048
	global_load_ushort v107, v[28:29], off offset:-4096
	global_load_ushort v105, v[28:29], off
	global_load_ushort v104, v[28:29], off offset:2048
	global_load_ushort v106, v[32:33], off offset:-4096
	global_load_ushort v103, v[32:33], off
	global_load_ushort v102, v[32:33], off offset:2048
	v_add_co_u32_e32 v28, vcc, s6, v12
	v_readfirstlane_b32 s15, v10
	s_nop 0
	v_addc_co_u32_e32 v29, vcc, 0, v13, vcc
	global_load_ushort v117, v[12:13], off
	global_load_ushort v116, v[12:13], off offset:2048
	global_load_ushort v115, v[24:25], off offset:-4096
	global_load_ushort v114, v[16:17], off offset:2048
	global_load_ushort v113, v[26:27], off offset:2048
	global_load_ushort v112, v[30:31], off offset:2048
	global_load_ushort v111, v[28:29], off
	global_load_ushort v110, v[28:29], off offset:2048
	v_lshl_add_u64 v[26:27], v[10:11], 2, s[12:13]
	s_ashr_i32 s13, s15, 2
	s_movk_i32 s10, 0x80
	s_and_b32 s12, s13, -16
	v_bfe_u32 v12, v10, 4, 2
	v_and_b32_e32 v13, 15, v10
	v_lshl_add_u32 v96, v10, 2, s14
	v_cmp_gt_u32_e64 s[10:11], s10, v10
	v_bfi_b32 v10, -16, s13, v10
	s_ashr_i32 s13, s12, 31
	s_lshl_b64 s[12:13], s[12:13], 1
	s_movk_i32 s16, 0x90
	s_add_u32 s2, s2, s12
	v_add_u32_e32 v16, s14, v34
	v_lshl_add_u64 v[24:25], s[4:5], 0, v[34:35]
	v_mov_b32_e32 v17, s14
	v_cmp_lt_i32_e64 s[4:5], 0, v36
	v_cmp_lt_i32_e64 s[6:7], 1, v36
	v_cmp_lt_i32_e64 s[8:9], 2, v36
	v_lshlrev_b32_e32 v32, 5, v36
	v_mul_lo_u32 v10, v10, s16
	v_lshlrev_b32_e32 v36, 4, v12
	s_addc_u32 s3, s3, s13
	v_lshlrev_b32_e32 v34, 3, v12
	v_lshl_add_u32 v97, v37, 2, s14
	v_mad_u32_u24 v17, v37, s16, v17
	v_add_u32_e32 v33, s14, v10
	v_add_u32_e32 v37, s14, v36
	v_lshl_add_u64 v[10:11], s[2:3], 0, v[34:35]
	v_lshl_add_u64 v[28:29], s[0:1], 0, v[14:15]
	v_mul_lo_u32 v12, v18, s16
	v_mul_lo_u32 v14, v20, s16
	v_mul_u32_u24_e32 v15, 0x90, v13
	v_lshlrev_b32_e32 v34, 8, v13
	v_lshl_add_u64 v[30:31], v[10:11], 0, v[34:35]
	v_add_u32_e32 v34, v16, v12
	v_add_u32_e32 v98, v16, v14
	v_add_u32_e32 v99, v17, v32
	v_add_u32_e32 v100, v33, v36
	v_add_u32_e32 v101, v37, v15
	s_branch .LBB0_945

; #define C1_PF_LF(ITEM, DIR) do { const int b_ = (ITEM) >> 7, h_ = ((ITEM) >> 5) & 3, j_ = (ITEM) & 31; const size_t tk_ = (size_t)b_ * SEQ + j_ * 64; \
;         _Pragma("unroll") for (int i = 0; i < 16; ++i) lfn[i] = (unsigned)((const unsigned short*)LF)[(tk_ + tq * 16 + i) * 1024 + (DIR) * 512 + h_ * 128 + d]; } while (0)
; __device__ __forceinline__ void c1_phase(LAS unsigned char* lds, const bf16_t* __restrict__ LF, const bf16_t* __restrict__ VTH, bf16_t* __restrict__ UT, float* __restrict__ DEC, int first, int count, int stride) {
;     ...
;         for (int dir = 0; dir < 2; ++dir) {
;             float lfv[16], cs[16];
; #pragma unroll
;             for (int i = 0; i < 16; ++i) lfv[i] = __uint_as_float(lfn[i] << 16);
;             if (dir == 0) C1_PF_LF(item, 1); else if (it + 1 < count) C1_PF_LF(item + stride, 0);
.LBB0_951:
	s_xor_b64 s[12:13], s[14:15], -1
	v_readfirstlane_b32 vcc_lo, v255
	s_cmp_lg_u32 vcc_lo, 0
	s_cbranch_scc1 .Lc1_steady
	s_waitcnt vmcnt(7)
	v_mov_b32_e32 v10, v117
	s_waitcnt vmcnt(6)
	v_mov_b32_e32 v11, v116
	s_waitcnt vmcnt(5)
	v_mov_b32_e32 v12, v115
	s_waitcnt vmcnt(4)
	v_mov_b32_e32 v13, v114
	v_mov_b32_e32 v14, v109
	v_mov_b32_e32 v15, v108
	v_mov_b32_e32 v16, v107
	s_waitcnt vmcnt(3)
	v_mov_b32_e32 v17, v113
	v_mov_b32_e32 v94, v105
	v_mov_b32_e32 v95, v104
	v_mov_b32_e32 v118, v106
	s_waitcnt vmcnt(2)
	v_mov_b32_e32 v119, v112
	v_mov_b32_e32 v120, v103
	v_mov_b32_e32 v121, v102
	s_waitcnt vmcnt(1)
	v_mov_b32_e32 v122, v111
	s_waitcnt vmcnt(0)
	v_mov_b32_e32 v123, v110
	s_branch .Lc1_join
.Lc1_steady:
	s_waitcnt vmcnt(15)
	v_mov_b32_e32 v10, v117
	s_waitcnt vmcnt(14)
	v_mov_b32_e32 v11, v116
	s_waitcnt vmcnt(13)
	v_mov_b32_e32 v12, v115
	s_waitcnt vmcnt(12)
	v_mov_b32_e32 v13, v114
	v_mov_b32_e32 v14, v109
	v_mov_b32_e32 v15, v108
	v_mov_b32_e32 v16, v107
	s_waitcnt vmcnt(11)
	v_mov_b32_e32 v17, v113
	v_mov_b32_e32 v94, v105
	v_mov_b32_e32 v95, v104
	v_mov_b32_e32 v118, v106
	s_waitcnt vmcnt(10)
	v_mov_b32_e32 v119, v112
	v_mov_b32_e32 v120, v103
	v_mov_b32_e32 v121, v102
	s_waitcnt vmcnt(9)
	v_mov_b32_e32 v122, v111
	s_waitcnt vmcnt(8)
	v_mov_b32_e32 v123, v110
.Lc1_join:
	v_mov_b32_e32 v255, 1
	s_and_b64 vcc, exec, s[12:13]
	s_mov_b64 s[16:17], -1
	s_cbranch_vccz .LBB0_955
	s_andn2_b64 vcc, exec, s[0:1]
	v_mov_b32_e32 v110, v123
	v_mov_b32_e32 v111, v122
	v_mov_b32_e32 v102, v121
	v_mov_b32_e32 v103, v120
	v_mov_b32_e32 v112, v119
	v_mov_b32_e32 v106, v118
	v_mov_b32_e32 v104, v95
	v_mov_b32_e32 v105, v94
	v_mov_b32_e32 v113, v17
	v_mov_b32_e32 v107, v16
	v_mov_b32_e32 v108, v15
	v_mov_b32_e32 v109, v14
	v_mov_b32_e32 v114, v13
	v_mov_b32_e32 v115, v12
	v_mov_b32_e32 v116, v11
	v_mov_b32_e32 v117, v10
	s_cbranch_vccnz .LBB0_954
	global_load_ushort v117, v[32:33], off
	global_load_ushort v116, v[32:33], off offset:2048
	global_load_ushort v115, v[36:37], off
	global_load_ushort v114, v[38:39], off
	global_load_ushort v109, v[40:41], off
	global_load_ushort v108, v[42:43], off
	global_load_ushort v107, v[44:45], off
	global_load_ushort v113, v[46:47], off
	global_load_ushort v105, v[48:49], off
	global_load_ushort v104, v[50:51], off
	global_load_ushort v106, v[52:53], off
	global_load_ushort v112, v[54:55], off
	global_load_ushort v103, v[56:57], off
	global_load_ushort v102, v[58:59], off
	global_load_ushort v111, v[60:61], off
	global_load_ushort v110, v[62:63], off
